# speedup vs baseline: 1.0112x; 1.0112x over previous
.LBB1_22:
	s_and_b64 vcc, exec, s[4:5]
	s_cbranch_vccz .LBB1_96
	s_setprio 2
	s_movk_i32 s3, 0x187
	v_cmp_gt_u32_e32 vcc, s3, v0
	s_movk_i32 s3, 0x186
	v_cmp_lt_u32_e64 s[4:5], s3, v0
	v_lshlrev_b32_e32 v40, 2, v0
	s_and_saveexec_b64 s[6:7], s[4:5]
	s_xor_b64 s[4:5], exec, s[6:7]
	v_lshlrev_b32_e32 v34, 2, v0
	s_or_saveexec_b64 s[6:7], s[4:5]
	s_load_dwordx8 s[12:19], s[0:1], 0x0
	s_load_dwordx2 s[20:21], s[0:1], 0x20
	s_xor_b64 exec, exec, s[6:7]
	s_cbranch_execz .LBB1_36
	s_movk_i32 s0, 0x87
	v_sub_u32_e64 v1, s0, v0 clamp
	v_add_u32_e32 v1, 0xff, v1
	v_lshrrev_b32_e32 v2, 8, v1
	s_mov_b32 s8, 0
	v_mov_b32_e32 v1, v2
	v_add_u32_e32 v3, 0x1040, v40
	s_mov_b32 s9, 1
	s_mov_b64 s[10:11], 0
	v_mov_b32_e32 v4, 0
	s_mov_b32 s22, s8
	s_branch .LBB1_28

.LBB2_22:
	s_and_b64 vcc, exec, s[4:5]
	s_cbranch_vccz .LBB2_275
	s_setprio 2
	s_load_dwordx2 s[8:9], s[0:1], 0x10
	s_movk_i32 s3, 0xc4
	v_cmp_gt_u32_e32 vcc, s3, v0
	v_mov_b32_e32 v4, 0
	v_mov_b32_e32 v1, 0
	s_and_saveexec_b64 s[4:5], vcc
	s_cbranch_execz .LBB2_25
	v_lshlrev_b32_e32 v1, 8, v0
	s_waitcnt lgkmcnt(0)
	global_load_dword v1, v1, s[8:9]
